# v048 + P17 epilogue: second-half bias/scale vectors loaded at the epilogue start (no wait behind the first half's stores)
# speedup vs baseline: 1.0045x; 1.0019x over previous
.LBB0_3162:
	s_lshl_b32 s1, s26, 2
	s_add_i32 s1, s1, 0
	s_ashr_i32 s27, s26, 31
	s_add_i32 s1, s1, 0x20480
	s_lshl_b64 s[28:29], s[26:27], 18
	s_add_u32 s28, s78, s28
	s_addc_u32 s29, s79, s29
	s_lshl_b64 s[26:27], s[26:27], 12
	s_add_u32 s30, s49, s26
	v_lshl_or_b32 v20, s24, 8, v206
	s_addc_u32 s31, s50, s27
	v_ashrrev_i32_e32 v21, 31, v20
	s_add_u32 s26, s47, s26
	s_nop 15
	s_nop 15
	v_lshlrev_b64 v[2:3], 2, v[20:21]
	s_addc_u32 s27, s48, s27
	v_lshl_add_u64 v[18:19], s[26:27], 0, v[2:3]
	v_mov_b32_e32 v4, s1
	global_load_dwordx4 v[10:13], v[18:19], off offset:16
	global_load_dwordx4 v[14:17], v[18:19], off
	ds_read_b32 v21, v4
	v_lshl_add_u64 v[22:23], s[30:31], 0, v[2:3]
	global_load_dwordx4 v[6:9], v[22:23], off
	global_load_dwordx4 v[2:5], v[22:23], off offset:16
	global_load_dwordx4 v[220:223], v[18:19], off offset:512
	global_load_dwordx4 v[224:227], v[18:19], off offset:528
	global_load_dwordx4 v[228:231], v[22:23], off offset:512
	global_load_dwordx4 v[232:235], v[22:23], off offset:528
	v_lshl_add_u32 v219, s22, 8, v1
	v_sub_u32_e32 v32, v20, v175
	s_waitcnt lgkmcnt(0)
	v_sub_u32_e32 v21, s22, v21
	v_lshl_add_u32 v24, v21, 8, v1
	v_ashrrev_i32_e32 v25, 31, v24
	v_lshl_add_u64 v[24:25], v[24:25], 2, s[28:29]
	global_load_dword v26, v[24:25], off
	global_load_dword v27, v[24:25], off offset:64
	global_load_dword v29, v[24:25], off offset:128
	global_load_dword v214, v[24:25], off offset:192
	global_load_dword v215, v[24:25], off offset:512
	global_load_dword v216, v[24:25], off offset:576
	global_load_dword v217, v[24:25], off offset:640
	global_load_dword v218, v[24:25], off offset:704
	v_or_b32_e32 v20, v219, v188
	v_ashrrev_i32_e32 v21, 31, v20
	v_lshlrev_b64 v[20:21], 10, v[20:21]
	v_ashrrev_i32_e32 v33, 31, v32
	v_lshl_add_u64 v[20:21], s[92:93], 0, v[20:21]
	s_nop 0
	v_lshl_add_u64 v[24:25], v[20:21], 0, v[32:33]
	s_nop 0
	s_nop 0
	s_nop 0
	s_andn2_b64 vcc, exec, s[14:15]
	s_mov_b64 s[14:15], -1
	s_waitcnt vmcnt(0)
	v_pk_mul_f32 v[212:213], v[10:11], s[8:9] op_sel_hi:[1,0]
	v_pk_mul_f32 v[184:185], v[16:17], s[8:9] op_sel_hi:[1,0]
	v_pk_mul_f32 v[186:187], v[14:15], s[8:9] op_sel_hi:[1,0]
	v_pk_fma_f32 v[30:31], v[160:161], v[184:185], v[8:9]
	v_pk_fma_f32 v[154:155], v[154:155], v[212:213], v[2:3]
	v_pk_fma_f32 v[160:161], v[146:147], v[212:213], v[2:3]
	v_mul_f32_e32 v146, 4.0, v26
	v_pk_fma_f32 v[158:159], v[158:159], v[186:187], v[6:7]
	v_pk_mul_f32 v[154:155], v[146:147], v[154:155] op_sel_hi:[0,1]
	v_mul_f32_e32 v28, 4.0, v27
	v_pk_mul_f32 v[158:159], v[146:147], v[158:159] op_sel_hi:[0,1]
	v_med3_f32 v21, v154, s57, v209
	v_med3_f32 v27, v155, s57, v209
	v_pk_mul_f32 v[210:211], v[12:13], s[8:9] op_sel_hi:[1,0]
	v_med3_f32 v11, v158, s57, v209
	v_med3_f32 v13, v159, s57, v209
	v_cvt_pk_fp8_f32 v181, v21, v27
	v_pk_fma_f32 v[156:157], v[156:157], v[210:211], v[4:5]
	v_pk_fma_f32 v[150:151], v[150:151], v[186:187], v[6:7]
	v_cvt_pk_fp8_f32 v180, v11, v13
	v_pk_fma_f32 v[152:153], v[152:153], v[184:185], v[8:9]
	v_pk_fma_f32 v[148:149], v[148:149], v[210:211], v[4:5]
	v_mul_f32_e32 v26, 4.0, v29
	v_pk_mul_f32 v[30:31], v[146:147], v[30:31] op_sel_hi:[0,1]
	v_pk_mul_f32 v[156:157], v[146:147], v[156:157] op_sel_hi:[0,1]
	v_pk_mul_f32 v[150:151], v[28:29], v[150:151] op_sel_hi:[0,1]
	v_pk_fma_f32 v[142:143], v[142:143], v[186:187], v[6:7]
	v_pk_mul_f32 v[152:153], v[28:29], v[152:153] op_sel_hi:[0,1]
	v_pk_mul_f32 v[160:161], v[28:29], v[160:161] op_sel_hi:[0,1]
	v_pk_mul_f32 v[148:149], v[28:29], v[148:149] op_sel_hi:[0,1]
	v_med3_f32 v15, v30, s57, v209
	v_med3_f32 v17, v31, s57, v209
	v_med3_f32 v29, v156, s57, v209
	v_med3_f32 v30, v157, s57, v209
	v_med3_f32 v31, v150, s57, v209
	v_med3_f32 v147, v151, s57, v209
	v_pk_mul_f32 v[142:143], v[26:27], v[142:143] op_sel_hi:[0,1]
	v_pk_fma_f32 v[138:139], v[138:139], v[212:213], v[2:3]
	v_cvt_pk_fp8_f32 v182, v31, v147
	v_cvt_pk_fp8_f32 v181, v29, v30 op_sel:[0,0,1]
	v_pk_fma_f32 v[30:31], v[144:145], v[184:185], v[8:9]
	v_pk_mul_f32 v[144:145], v[26:27], v[138:139] op_sel_hi:[0,1]
	v_med3_f32 v11, v142, s57, v209
	v_med3_f32 v13, v143, s57, v209
	s_nop 0
	v_cvt_pk_fp8_f32 v180, v15, v17 op_sel:[0,0,1]
	v_cvt_pk_fp8_f32 v138, v11, v13
	v_med3_f32 v15, v144, s57, v209
	v_med3_f32 v17, v145, s57, v209
	s_nop 0
	v_cvt_pk_fp8_f32 v139, v15, v17
	v_pk_mul_f32 v[30:31], v[26:27], v[30:31] op_sel_hi:[0,1]
	v_pk_fma_f32 v[140:141], v[140:141], v[210:211], v[4:5]
	v_mul_f32_e32 v20, 4.0, v214
	v_pk_mul_f32 v[140:141], v[26:27], v[140:141] op_sel_hi:[0,1]
	v_med3_f32 v11, v30, s57, v209
	v_med3_f32 v13, v31, s57, v209
	v_pk_fma_f32 v[134:135], v[134:135], v[186:187], v[6:7]
	v_cvt_pk_fp8_f32 v138, v11, v13 op_sel:[0,0,1]
	v_med3_f32 v11, v140, s57, v209
	v_med3_f32 v13, v141, s57, v209
	v_pk_mul_f32 v[134:135], v[20:21], v[134:135] op_sel_hi:[0,1]
	v_pk_fma_f32 v[130:131], v[130:131], v[212:213], v[2:3]
	v_cvt_pk_fp8_f32 v139, v11, v13 op_sel:[0,0,1]
	v_pk_mul_f32 v[130:131], v[20:21], v[130:131] op_sel_hi:[0,1]
	v_med3_f32 v11, v134, s57, v209
	v_med3_f32 v13, v135, s57, v209
	s_nop 0
	v_cvt_pk_fp8_f32 v140, v11, v13
	v_med3_f32 v15, v130, s57, v209
	v_med3_f32 v17, v131, s57, v209
	s_nop 0
	v_pk_fma_f32 v[30:31], v[136:137], v[184:185], v[8:9]
	v_cvt_pk_fp8_f32 v141, v15, v17
	v_pk_mul_f32 v[30:31], v[20:21], v[30:31] op_sel_hi:[0,1]
	v_pk_fma_f32 v[132:133], v[132:133], v[210:211], v[4:5]
	v_mul_f32_e32 v16, 4.0, v215
	v_pk_mul_f32 v[132:133], v[20:21], v[132:133] op_sel_hi:[0,1]
	v_med3_f32 v11, v30, s57, v209
	v_med3_f32 v13, v31, s57, v209
	v_pk_fma_f32 v[126:127], v[126:127], v[186:187], v[6:7]
	v_cvt_pk_fp8_f32 v140, v11, v13 op_sel:[0,0,1]
	v_med3_f32 v11, v132, s57, v209
	v_med3_f32 v13, v133, s57, v209
	v_pk_mul_f32 v[126:127], v[16:17], v[126:127] op_sel_hi:[0,1]
	v_pk_fma_f32 v[122:123], v[122:123], v[212:213], v[2:3]
	v_cvt_pk_fp8_f32 v141, v11, v13 op_sel:[0,0,1]
	v_pk_mul_f32 v[130:131], v[16:17], v[122:123] op_sel_hi:[0,1]
	v_med3_f32 v13, v126, s57, v209
	v_med3_f32 v15, v127, s57, v209
	s_nop 0
	v_pk_fma_f32 v[128:129], v[128:129], v[184:185], v[8:9]
	v_pk_fma_f32 v[124:125], v[124:125], v[210:211], v[4:5]
	v_cvt_pk_fp8_f32 v122, v13, v15
	v_pk_mul_f32 v[128:129], v[16:17], v[128:129] op_sel_hi:[0,1]
	v_pk_mul_f32 v[124:125], v[16:17], v[124:125] op_sel_hi:[0,1]
	v_med3_f32 v17, v130, s57, v209
	v_med3_f32 v21, v131, s57, v209
	s_nop 0
	v_cvt_pk_fp8_f32 v123, v17, v21
	v_med3_f32 v13, v128, s57, v209
	v_med3_f32 v15, v129, s57, v209
	v_mul_f32_e32 v14, 4.0, v216
	v_cvt_pk_fp8_f32 v122, v13, v15 op_sel:[0,0,1]
	v_med3_f32 v15, v125, s57, v209
	v_pk_fma_f32 v[118:119], v[118:119], v[186:187], v[6:7]
	v_med3_f32 v13, v124, s57, v209
	v_pk_fma_f32 v[120:121], v[120:121], v[184:185], v[8:9]
	v_pk_mul_f32 v[118:119], v[14:15], v[118:119] op_sel_hi:[0,1]
	v_pk_fma_f32 v[116:117], v[116:117], v[210:211], v[4:5]
	v_pk_fma_f32 v[114:115], v[114:115], v[212:213], v[2:3]
	v_cvt_pk_fp8_f32 v123, v13, v15 op_sel:[0,0,1]
	v_pk_mul_f32 v[120:121], v[14:15], v[120:121] op_sel_hi:[0,1]
	v_pk_mul_f32 v[114:115], v[14:15], v[114:115] op_sel_hi:[0,1]
	v_pk_mul_f32 v[116:117], v[14:15], v[116:117] op_sel_hi:[0,1]
	v_med3_f32 v13, v118, s57, v209
	v_med3_f32 v15, v119, s57, v209
	s_nop 0
	v_cvt_pk_fp8_f32 v124, v13, v15
	v_med3_f32 v17, v114, s57, v209
	v_med3_f32 v21, v115, s57, v209
	s_nop 0
	v_cvt_pk_fp8_f32 v125, v17, v21
	v_med3_f32 v13, v120, s57, v209
	v_med3_f32 v15, v121, s57, v209
	v_mul_f32_e32 v12, 4.0, v217
	v_cvt_pk_fp8_f32 v124, v13, v15 op_sel:[0,0,1]
	v_med3_f32 v13, v116, s57, v209
	v_pk_fma_f32 v[110:111], v[110:111], v[186:187], v[6:7]
	v_med3_f32 v15, v117, s57, v209
	v_pk_fma_f32 v[112:113], v[112:113], v[184:185], v[8:9]
	v_pk_mul_f32 v[110:111], v[12:13], v[110:111] op_sel_hi:[0,1]
	v_pk_fma_f32 v[108:109], v[108:109], v[210:211], v[4:5]
	v_pk_fma_f32 v[106:107], v[106:107], v[212:213], v[2:3]
	v_cvt_pk_fp8_f32 v125, v13, v15 op_sel:[0,0,1]
	v_pk_mul_f32 v[112:113], v[12:13], v[112:113] op_sel_hi:[0,1]
	v_pk_mul_f32 v[116:117], v[12:13], v[106:107] op_sel_hi:[0,1]
	v_pk_mul_f32 v[108:109], v[12:13], v[108:109] op_sel_hi:[0,1]
	v_med3_f32 v13, v110, s57, v209
	v_med3_f32 v15, v111, s57, v209
	s_nop 0
	v_cvt_pk_fp8_f32 v106, v13, v15
	v_mul_f32_e32 v10, 4.0, v218
	v_add_u32_e32 v11, 0x80, v219
	v_pk_fma_f32 v[6:7], v[102:103], v[186:187], v[6:7]
	v_pk_fma_f32 v[2:3], v[94:95], v[212:213], v[2:3]
	v_med3_f32 v13, v112, s57, v209
	v_med3_f32 v15, v113, s57, v209
	v_pk_mul_f32 v[6:7], v[10:11], v[6:7] op_sel_hi:[0,1]
	v_pk_mul_f32 v[2:3], v[10:11], v[2:3] op_sel_hi:[0,1]
	v_med3_f32 v150, v152, s57, v209
	v_med3_f32 v151, v153, s57, v209
	v_med3_f32 v152, v160, s57, v209
	v_med3_f32 v153, v161, s57, v209
	v_med3_f32 v17, v116, s57, v209
	v_med3_f32 v21, v117, s57, v209
	s_nop 0
	v_cvt_pk_fp8_f32 v106, v13, v15 op_sel:[0,0,1]
	v_med3_f32 v13, v108, s57, v209
	v_med3_f32 v15, v109, s57, v209
	v_med3_f32 v6, v6, s57, v209
	v_med3_f32 v7, v7, s57, v209
	s_nop 0
	v_med3_f32 v2, v2, s57, v209
	v_med3_f32 v3, v3, s57, v209
	s_nop 0
	v_cvt_pk_fp8_f32 v183, v152, v153
	v_cvt_pk_fp8_f32 v107, v17, v21
	v_cvt_pk_fp8_f32 v108, v6, v7
	v_cvt_pk_fp8_f32 v109, v2, v3
	v_pk_fma_f32 v[8:9], v[104:105], v[184:185], v[8:9]
	v_pk_fma_f32 v[4:5], v[96:97], v[210:211], v[4:5]
	v_pk_mul_f32 v[8:9], v[10:11], v[8:9] op_sel_hi:[0,1]
	v_pk_mul_f32 v[4:5], v[10:11], v[4:5] op_sel_hi:[0,1]
	v_med3_f32 v148, v148, s57, v209
	v_med3_f32 v149, v149, s57, v209
	v_med3_f32 v6, v8, s57, v209
	v_med3_f32 v7, v9, s57, v209
	v_med3_f32 v2, v4, s57, v209
	v_med3_f32 v3, v5, s57, v209
	v_cvt_pk_fp8_f32 v182, v150, v151 op_sel:[0,0,1]
	v_cvt_pk_fp8_f32 v183, v148, v149 op_sel:[0,0,1]
	v_or_b32_e32 v30, v219, v189
	v_or_b32_e32 v114, v11, v188
	v_cvt_pk_fp8_f32 v107, v13, v15 op_sel:[0,0,1]
	v_cvt_pk_fp8_f32 v108, v6, v7 op_sel:[0,0,1]
	v_cvt_pk_fp8_f32 v109, v2, v3 op_sel:[0,0,1]
	v_or_b32_e32 v2, v11, v189
	v_ashrrev_i32_e32 v31, 31, v30
	v_ashrrev_i32_e32 v115, 31, v114
	v_ashrrev_i32_e32 v3, 31, v2
	v_lshlrev_b64 v[30:31], 10, v[30:31]
	v_lshlrev_b64 v[114:115], 10, v[114:115]
	v_lshlrev_b64 v[2:3], 10, v[2:3]
	v_lshl_add_u64 v[30:31], s[92:93], 0, v[30:31]
	v_lshl_add_u64 v[114:115], s[92:93], 0, v[114:115]
	v_lshl_add_u64 v[2:3], s[92:93], 0, v[2:3]
	v_permlane16_swap_b32_e32 v180, v182
	v_permlane16_swap_b32_e32 v181, v183
	v_permlane16_swap_b32_e32 v138, v140
	v_permlane16_swap_b32_e32 v139, v141
	v_lshl_add_u64 v[30:31], v[30:31], 0, v[32:33]
	v_permlane16_swap_b32_e32 v122, v124
	v_permlane16_swap_b32_e32 v123, v125
	v_lshl_add_u64 v[114:115], v[114:115], 0, v[32:33]
	v_permlane16_swap_b32_e32 v106, v108
	v_permlane16_swap_b32_e32 v107, v109
	v_lshl_add_u64 v[32:33], v[2:3], 0, v[32:33]
	global_store_dwordx4 v[24:25], v[180:183], off
	global_store_dwordx4 v[30:31], v[138:141], off
	global_store_dwordx4 v[114:115], v[122:125], off
	global_store_dwordx4 v[32:33], v[106:109], off
	s_nop 0
	v_pk_mul_f32 v[220:221], v[220:221], s[8:9] op_sel_hi:[1,0]
	s_nop 0
	v_pk_mul_f32 v[224:225], v[224:225], s[8:9] op_sel_hi:[1,0]
	s_nop 0
	v_pk_fma_f32 v[98:99], v[98:99], v[220:221], v[228:229]
	v_pk_mul_f32 v[22:23], v[222:223], s[8:9] op_sel_hi:[1,0]
	v_pk_mul_f32 v[98:99], v[146:147], v[98:99] op_sel_hi:[0,1]
	s_nop 0
	v_pk_fma_f32 v[90:91], v[90:91], v[224:225], v[232:233]
	v_pk_fma_f32 v[18:19], v[100:101], v[22:23], v[230:231]
	v_pk_mul_f32 v[100:101], v[146:147], v[90:91] op_sel_hi:[0,1]
	v_med3_f32 v11, v98, s57, v209
	v_med3_f32 v13, v99, s57, v209
	s_nop 0
	v_cvt_pk_fp8_f32 v90, v11, v13
	v_med3_f32 v15, v100, s57, v209
	v_med3_f32 v17, v101, s57, v209
	s_nop 0
	v_pk_mul_f32 v[222:223], v[226:227], s[8:9] op_sel_hi:[1,0]
	v_cvt_pk_fp8_f32 v91, v15, v17
	v_pk_mul_f32 v[18:19], v[146:147], v[18:19] op_sel_hi:[0,1]
	v_pk_fma_f32 v[92:93], v[92:93], v[222:223], v[234:235]
	v_med3_f32 v11, v18, s57, v209
	v_pk_mul_f32 v[92:93], v[146:147], v[92:93] op_sel_hi:[0,1]
	v_med3_f32 v13, v19, s57, v209
	v_pk_fma_f32 v[86:87], v[86:87], v[220:221], v[228:229]
	v_cvt_pk_fp8_f32 v90, v11, v13 op_sel:[0,0,1]
	v_med3_f32 v11, v92, s57, v209
	v_med3_f32 v13, v93, s57, v209
	v_pk_mul_f32 v[86:87], v[28:29], v[86:87] op_sel_hi:[0,1]
	v_pk_fma_f32 v[82:83], v[82:83], v[224:225], v[232:233]
	v_cvt_pk_fp8_f32 v91, v11, v13 op_sel:[0,0,1]
	v_pk_mul_f32 v[82:83], v[28:29], v[82:83] op_sel_hi:[0,1]
	v_med3_f32 v11, v86, s57, v209
	v_med3_f32 v13, v87, s57, v209
	s_nop 0
	v_cvt_pk_fp8_f32 v92, v11, v13
	v_med3_f32 v15, v82, s57, v209
	v_med3_f32 v17, v83, s57, v209
	s_nop 0
	v_pk_fma_f32 v[18:19], v[88:89], v[22:23], v[230:231]
	v_cvt_pk_fp8_f32 v93, v15, v17
	v_pk_mul_f32 v[18:19], v[28:29], v[18:19] op_sel_hi:[0,1]
	v_pk_fma_f32 v[84:85], v[84:85], v[222:223], v[234:235]
	v_med3_f32 v11, v18, s57, v209
	v_pk_mul_f32 v[28:29], v[28:29], v[84:85] op_sel_hi:[0,1]
	v_med3_f32 v13, v19, s57, v209
	v_cvt_pk_fp8_f32 v92, v11, v13 op_sel:[0,0,1]
	v_med3_f32 v11, v28, s57, v209
	v_med3_f32 v13, v29, s57, v209
	v_cvt_pk_fp8_f32 v93, v11, v13 op_sel:[0,0,1]
	v_permlane16_swap_b32_e32 v90, v92
	v_pk_fma_f32 v[18:19], v[80:81], v[22:23], v[230:231]
	v_permlane16_swap_b32_e32 v91, v93
	global_store_dwordx4 v[24:25], v[90:93], off offset:128
	v_pk_fma_f32 v[24:25], v[78:79], v[220:221], v[228:229]
	v_pk_mul_f32 v[28:29], v[26:27], v[18:19] op_sel_hi:[0,1]
	v_pk_mul_f32 v[24:25], v[26:27], v[24:25] op_sel_hi:[0,1]
	v_pk_fma_f32 v[18:19], v[76:77], v[222:223], v[234:235]
	v_pk_fma_f32 v[74:75], v[74:75], v[224:225], v[232:233]
	v_med3_f32 v11, v24, s57, v209
	v_pk_mul_f32 v[74:75], v[26:27], v[74:75] op_sel_hi:[0,1]
	v_pk_mul_f32 v[26:27], v[26:27], v[18:19] op_sel_hi:[0,1]
	v_med3_f32 v13, v25, s57, v209
	s_nop 0
	v_cvt_pk_fp8_f32 v18, v11, v13
	v_med3_f32 v15, v74, s57, v209
	v_med3_f32 v17, v75, s57, v209
	s_nop 0
	v_cvt_pk_fp8_f32 v19, v15, v17
	v_med3_f32 v11, v28, s57, v209
	v_med3_f32 v13, v29, s57, v209
	v_cvt_pk_fp8_f32 v18, v11, v13 op_sel:[0,0,1]
	v_med3_f32 v11, v26, s57, v209
	v_med3_f32 v13, v27, s57, v209
	v_pk_fma_f32 v[26:27], v[62:63], v[220:221], v[228:229]
	v_pk_fma_f32 v[24:25], v[64:65], v[22:23], v[230:231]
	v_pk_mul_f32 v[26:27], v[20:21], v[26:27] op_sel_hi:[0,1]
	v_pk_fma_f32 v[28:29], v[52:53], v[222:223], v[234:235]
	v_pk_fma_f32 v[50:51], v[50:51], v[224:225], v[232:233]
	v_cvt_pk_fp8_f32 v19, v11, v13 op_sel:[0,0,1]
	v_pk_mul_f32 v[24:25], v[20:21], v[24:25] op_sel_hi:[0,1]
	v_pk_mul_f32 v[50:51], v[20:21], v[50:51] op_sel_hi:[0,1]
	v_pk_mul_f32 v[28:29], v[20:21], v[28:29] op_sel_hi:[0,1]
	v_med3_f32 v11, v26, s57, v209
	v_med3_f32 v13, v27, s57, v209
	s_nop 0
	v_cvt_pk_fp8_f32 v20, v11, v13
	v_med3_f32 v15, v50, s57, v209
	v_med3_f32 v17, v51, s57, v209
	s_nop 0
	v_cvt_pk_fp8_f32 v21, v15, v17
	v_med3_f32 v11, v24, s57, v209
	v_med3_f32 v13, v25, s57, v209
	v_cvt_pk_fp8_f32 v20, v11, v13 op_sel:[0,0,1]
	v_med3_f32 v11, v28, s57, v209
	v_med3_f32 v13, v29, s57, v209
	v_cvt_pk_fp8_f32 v21, v11, v13 op_sel:[0,0,1]
	v_permlane16_swap_b32_e32 v18, v20
	v_pk_fma_f32 v[24:25], v[68:69], v[222:223], v[234:235]
	v_permlane16_swap_b32_e32 v19, v21
	global_store_dwordx4 v[30:31], v[18:21], off offset:128
	v_pk_fma_f32 v[26:27], v[66:67], v[224:225], v[232:233]
	v_pk_mul_f32 v[24:25], v[16:17], v[24:25] op_sel_hi:[0,1]
	v_pk_fma_f32 v[20:21], v[70:71], v[220:221], v[228:229]
	v_pk_fma_f32 v[18:19], v[72:73], v[22:23], v[230:231]
	v_pk_mul_f32 v[20:21], v[16:17], v[20:21] op_sel_hi:[0,1]
	v_pk_mul_f32 v[18:19], v[16:17], v[18:19] op_sel_hi:[0,1]
	v_pk_mul_f32 v[26:27], v[16:17], v[26:27] op_sel_hi:[0,1]
	v_med3_f32 v11, v20, s57, v209
	v_med3_f32 v13, v21, s57, v209
	s_nop 0
	v_cvt_pk_fp8_f32 v16, v11, v13
	v_med3_f32 v11, v18, s57, v209
	v_med3_f32 v15, v26, s57, v209
	v_med3_f32 v18, v27, s57, v209
	s_nop 0
	v_cvt_pk_fp8_f32 v17, v15, v18
	v_med3_f32 v13, v19, s57, v209
	v_pk_fma_f32 v[18:19], v[60:61], v[22:23], v[230:231]
	v_pk_fma_f32 v[20:21], v[58:59], v[220:221], v[228:229]
	v_cvt_pk_fp8_f32 v16, v11, v13 op_sel:[0,0,1]
	v_med3_f32 v11, v24, s57, v209
	v_med3_f32 v13, v25, s57, v209
	v_pk_mul_f32 v[20:21], v[14:15], v[20:21] op_sel_hi:[0,1]
	v_pk_mul_f32 v[24:25], v[14:15], v[18:19] op_sel_hi:[0,1]
	v_pk_fma_f32 v[18:19], v[56:57], v[222:223], v[234:235]
	v_pk_fma_f32 v[26:27], v[54:55], v[224:225], v[232:233]
	v_cvt_pk_fp8_f32 v17, v11, v13 op_sel:[0,0,1]
	v_pk_mul_f32 v[26:27], v[14:15], v[26:27] op_sel_hi:[0,1]
	v_pk_mul_f32 v[14:15], v[14:15], v[18:19] op_sel_hi:[0,1]
	v_med3_f32 v11, v20, s57, v209
	v_med3_f32 v13, v21, s57, v209
	s_nop 0
	v_cvt_pk_fp8_f32 v18, v11, v13
	v_med3_f32 v20, v26, s57, v209
	v_med3_f32 v21, v27, s57, v209
	s_nop 0
	v_cvt_pk_fp8_f32 v19, v20, v21
	v_med3_f32 v11, v24, s57, v209
	v_med3_f32 v13, v25, s57, v209
	v_cvt_pk_fp8_f32 v18, v11, v13 op_sel:[0,0,1]
	v_med3_f32 v11, v14, s57, v209
	v_med3_f32 v13, v15, s57, v209
	v_cvt_pk_fp8_f32 v19, v11, v13 op_sel:[0,0,1]
	v_permlane16_swap_b32_e32 v16, v18
	v_pk_fma_f32 v[14:15], v[48:49], v[22:23], v[230:231]
	v_permlane16_swap_b32_e32 v17, v19
	global_store_dwordx4 v[114:115], v[16:19], off offset:128
	v_pk_fma_f32 v[20:21], v[42:43], v[224:225], v[232:233]
	v_pk_mul_f32 v[14:15], v[12:13], v[14:15] op_sel_hi:[0,1]
	v_pk_fma_f32 v[16:17], v[46:47], v[220:221], v[228:229]
	v_pk_fma_f32 v[18:19], v[44:45], v[222:223], v[234:235]
	v_pk_mul_f32 v[16:17], v[12:13], v[16:17] op_sel_hi:[0,1]
	v_pk_mul_f32 v[20:21], v[12:13], v[20:21] op_sel_hi:[0,1]
	v_pk_mul_f32 v[18:19], v[12:13], v[18:19] op_sel_hi:[0,1]
	v_med3_f32 v11, v16, s57, v209
	v_med3_f32 v13, v17, s57, v209
	s_nop 0
	v_cvt_pk_fp8_f32 v12, v11, v13
	v_med3_f32 v11, v14, s57, v209
	v_med3_f32 v14, v15, s57, v209
	v_med3_f32 v15, v20, s57, v209
	v_med3_f32 v16, v21, s57, v209
	s_nop 0
	v_cvt_pk_fp8_f32 v13, v15, v16
	v_cvt_pk_fp8_f32 v12, v11, v14 op_sel:[0,0,1]
	v_med3_f32 v11, v18, s57, v209
	v_pk_fma_f32 v[228:229], v[38:39], v[220:221], v[228:229]
	v_pk_fma_f32 v[232:233], v[34:35], v[224:225], v[232:233]
	v_med3_f32 v14, v19, s57, v209
	v_pk_mul_f32 v[228:229], v[10:11], v[228:229] op_sel_hi:[0,1]
	v_pk_mul_f32 v[232:233], v[10:11], v[232:233] op_sel_hi:[0,1]
	v_cvt_pk_fp8_f32 v13, v11, v14 op_sel:[0,0,1]
	v_med3_f32 v228, v228, s57, v209
	v_med3_f32 v229, v229, s57, v209
	s_nop 0
	v_med3_f32 v232, v232, s57, v209
	v_med3_f32 v233, v233, s57, v209
	s_nop 0
	v_cvt_pk_fp8_f32 v14, v228, v229
	v_cvt_pk_fp8_f32 v15, v232, v233
	v_pk_fma_f32 v[230:231], v[40:41], v[22:23], v[230:231]
	v_pk_fma_f32 v[234:235], v[36:37], v[222:223], v[234:235]
	v_pk_mul_f32 v[230:231], v[10:11], v[230:231] op_sel_hi:[0,1]
	v_pk_mul_f32 v[234:235], v[10:11], v[234:235] op_sel_hi:[0,1]
	v_med3_f32 v228, v230, s57, v209
	v_med3_f32 v229, v231, s57, v209
	v_med3_f32 v232, v234, s57, v209
	v_med3_f32 v233, v235, s57, v209
	v_cvt_pk_fp8_f32 v14, v228, v229 op_sel:[0,0,1]
	v_cvt_pk_fp8_f32 v15, v232, v233 op_sel:[0,0,1]
	s_nop 0
	v_permlane16_swap_b32_e32 v12, v14
	v_permlane16_swap_b32_e32 v13, v15
	global_store_dwordx4 v[32:33], v[12:15], off offset:128
	s_cbranch_vccnz .LBB0_3153
	s_andn2_b64 vcc, exec, s[2:3]
	s_cbranch_vccnz .LBB0_3152
	s_barrier
	s_branch .LBB0_3152
